# P3 load rebalancing: workgroups 0-15 (five prep items) do three uin tiles, their fourth tiles done in 16-row quarters by workgroups 16-79
# baseline (speedup 1.0000x reference)
.LBB0_469:
	s_cmpk_gt_i32 s92, 0x3ff
	v_readlane_b32 s56, v252, 59
	s_cbranch_scc1 .LBB0_506
	s_and_b32 s0, s62, 3
	s_cmp_lg_u32 s0, 0
	s_cbranch_scc1 .Luin_orig
	v_readlane_b32 s2, v252, 4
	v_readlane_b32 s3, v252, 5
	v_readlane_b32 s8, v252, 39
	v_readlane_b32 s9, v252, 40
	v_readlane_b32 s10, v252, 60
	v_readlane_b32 s11, v252, 61
	s_add_u32 s4, s2, 0x1eb00000
	s_addc_u32 s5, s3, 0
	s_add_u32 s6, s2, 0x2f700000
	s_addc_u32 s7, s3, 0
	s_mov_b32 s12, s92
	s_movk_i32 s27, 0x4000
	v_and_b32_e32 v1, 31, v0
	v_lshrrev_b32_e32 v2, 5, v0
	s_and_b32 s14, s12, 3
	s_lshl_b32 s14, s14, 8
	v_lshl_add_u32 v5, v1, 3, s14
	v_lshlrev_b32_e32 v5, 2, v5
	s_add_u32 s36, s8, 0x1000
	s_addc_u32 s37, s9, 0
	global_load_dwordx4 v[8:11], v5, s[36:37]
	global_load_dwordx4 v[12:15], v5, s[36:37] offset:16
	s_add_u32 s36, s8, 0x4000
	s_addc_u32 s37, s9, 0
	global_load_dwordx4 v[16:19], v5, s[36:37]
	global_load_dwordx4 v[20:23], v5, s[36:37] offset:16
	s_add_u32 s36, s8, 0x7000
	s_addc_u32 s37, s9, 0
	global_load_dwordx4 v[24:27], v5, s[36:37]
	global_load_dwordx4 v[28:31], v5, s[36:37] offset:16
	s_add_u32 s36, s10, 0x1000
	s_addc_u32 s37, s11, 0
	global_load_dwordx4 v[32:35], v5, s[36:37]
	global_load_dwordx4 v[36:39], v5, s[36:37] offset:16
	s_add_u32 s36, s8, 0x2000
	s_addc_u32 s37, s9, 0
	global_load_dwordx4 v[40:43], v5, s[36:37]
	global_load_dwordx4 v[44:47], v5, s[36:37] offset:16
	s_add_u32 s36, s8, 0x5000
	s_addc_u32 s37, s9, 0
	global_load_dwordx4 v[48:51], v5, s[36:37]
	global_load_dwordx4 v[52:55], v5, s[36:37] offset:16
	s_add_u32 s36, s8, 0x8000
	s_addc_u32 s37, s9, 0
	global_load_dwordx4 v[56:59], v5, s[36:37]
	global_load_dwordx4 v[60:63], v5, s[36:37] offset:16
	s_add_u32 s36, s10, 0x2000
	s_addc_u32 s37, s11, 0
	global_load_dwordx4 v[64:67], v5, s[36:37]
	global_load_dwordx4 v[68:71], v5, s[36:37] offset:16
	v_mul_u32_u24_e32 v6, 0x880, v1
	v_lshl_add_u32 v6, v2, 4, v6
	v_lshrrev_b32_e32 v126, 4, v0
	v_and_b32_e32 v127, 15, v0
	v_mul_u32_u24_e32 v7, 0x110, v126
	v_lshl_add_u32 v7, v127, 4, v7
	v_lshlrev_b32_e32 v164, 16, v126
	v_lshl_add_u32 v164, v127, 4, v164
	s_movk_i32 s26, 0x3200
	s_movk_i32 s20, 0x400
	s_mov_b32 s21, 0
	s_cmpk_lg_i32 s62, 0x100
	s_cbranch_scc1 .Luin_nobal
	s_cmpk_lt_u32 s92, 16
	s_cbranch_scc0 .Luin_b1
	s_movk_i32 s20, 0x300
.Luin_b1:
	s_sub_u32 s28, s92, 16
	s_cmpk_lt_u32 s28, 64
	s_cselect_b32 s21, 1, 0
.Luin_nobal:
	s_lshl_b32 s15, s14, 1
	s_add_u32 s15, s15, 0x2040
	s_lshr_b32 s13, s12, 2
	s_lshl_b32 s13, s13, 6
	v_lshl_add_u32 v3, v2, 2, s13
	v_add_u32_e32 v4, 4, v3
	v_add_u32_e32 v3, -1, v3
	v_mul_lo_u32 v165, v3, s26
	v_lshl_add_u32 v126, v1, 4, s15
	v_add_u32_e32 v165, v165, v126
	v_add_u32_e32 v166, 0x3200, v165
	v_add_u32_e32 v167, 0x3200, v166
	v_add_u32_e32 v168, 0x3200, v167
	v_add_u32_e32 v169, 0x3200, v168
	v_add_u32_e32 v170, 0x3200, v169
	v_mov_b32_e32 v72, 0
	v_mov_b32_e32 v73, 0
	v_mov_b32_e32 v74, 0
	v_mov_b32_e32 v75, 0
	v_mov_b32_e32 v92, 0
	v_mov_b32_e32 v93, 0
	v_mov_b32_e32 v94, 0
	v_mov_b32_e32 v95, 0
	v_mov_b32_e32 v96, 0
	v_mov_b32_e32 v97, 0
	v_mov_b32_e32 v98, 0
	v_mov_b32_e32 v99, 0
	v_mov_b32_e32 v116, 0
	v_mov_b32_e32 v117, 0
	v_mov_b32_e32 v118, 0
	v_mov_b32_e32 v119, 0
	global_load_dwordx4 v[76:79], v166, s[4:5]
	global_load_dwordx4 v[100:103], v166, s[4:5] offset:2048
	global_load_dwordx4 v[80:83], v167, s[4:5]
	global_load_dwordx4 v[104:107], v167, s[4:5] offset:2048
	global_load_dwordx4 v[84:87], v168, s[4:5]
	global_load_dwordx4 v[108:111], v168, s[4:5] offset:2048
	global_load_dwordx4 v[88:91], v169, s[4:5]
	global_load_dwordx4 v[112:115], v169, s[4:5] offset:2048
	v_cmp_le_i32_e32 vcc, 0, v3
	s_and_saveexec_b64 s[22:23], vcc
	global_load_dwordx4 v[72:75], v165, s[4:5]
	global_load_dwordx4 v[96:99], v165, s[4:5] offset:2048
	s_mov_b64 exec, s[22:23]
	v_cmp_gt_i32_e32 vcc, s27, v4
	s_and_saveexec_b64 s[22:23], vcc
	global_load_dwordx4 v[92:95], v170, s[4:5]
	global_load_dwordx4 v[116:119], v170, s[4:5] offset:2048
	s_mov_b64 exec, s[22:23]
	s_waitcnt vmcnt(0)
	s_branch .Luin_have

.Luin_have:
	v_lshlrev_b32_e32 v120, 16, v72
	v_lshlrev_b32_e32 v121, 16, v76
	v_lshlrev_b32_e32 v122, 16, v80
	v_lshlrev_b32_e32 v123, 16, v84
	v_lshlrev_b32_e32 v124, 16, v88
	v_lshlrev_b32_e32 v125, 16, v92
	v_mul_f32_e32 v126, v16, v121
	v_fmac_f32_e32 v126, v8, v120
	v_fmac_f32_e32 v126, v24, v122
	v_add_f32_e32 v132, v32, v126
	v_mul_f32_e32 v127, v16, v122
	v_fmac_f32_e32 v127, v8, v121
	v_fmac_f32_e32 v127, v24, v123
	v_add_f32_e32 v133, v32, v127
	v_mul_f32_e32 v128, v16, v123
	v_fmac_f32_e32 v128, v8, v122
	v_fmac_f32_e32 v128, v24, v124
	v_add_f32_e32 v134, v32, v128
	v_mul_f32_e32 v129, v16, v124
	v_fmac_f32_e32 v129, v8, v123
	v_fmac_f32_e32 v129, v24, v125
	v_add_f32_e32 v135, v32, v129
	v_and_b32_e32 v120, 0xffff0000, v72
	v_and_b32_e32 v121, 0xffff0000, v76
	v_and_b32_e32 v122, 0xffff0000, v80
	v_and_b32_e32 v123, 0xffff0000, v84
	v_and_b32_e32 v124, 0xffff0000, v88
	v_and_b32_e32 v125, 0xffff0000, v92
	v_mul_f32_e32 v126, v17, v121
	v_fmac_f32_e32 v126, v9, v120
	v_fmac_f32_e32 v126, v25, v122
	v_add_f32_e32 v136, v33, v126
	v_mul_f32_e32 v127, v17, v122
	v_fmac_f32_e32 v127, v9, v121
	v_fmac_f32_e32 v127, v25, v123
	v_add_f32_e32 v137, v33, v127
	v_mul_f32_e32 v128, v17, v123
	v_fmac_f32_e32 v128, v9, v122
	v_fmac_f32_e32 v128, v25, v124
	v_add_f32_e32 v138, v33, v128
	v_mul_f32_e32 v129, v17, v124
	v_fmac_f32_e32 v129, v9, v123
	v_fmac_f32_e32 v129, v25, v125
	v_add_f32_e32 v139, v33, v129
	v_lshlrev_b32_e32 v120, 16, v73
	v_lshlrev_b32_e32 v121, 16, v77
	v_lshlrev_b32_e32 v122, 16, v81
	v_lshlrev_b32_e32 v123, 16, v85
	v_lshlrev_b32_e32 v124, 16, v89
	v_lshlrev_b32_e32 v125, 16, v93
	v_mul_f32_e32 v126, v18, v121
	v_fmac_f32_e32 v126, v10, v120
	v_fmac_f32_e32 v126, v26, v122
	v_add_f32_e32 v140, v34, v126
	v_mul_f32_e32 v127, v18, v122
	v_fmac_f32_e32 v127, v10, v121
	v_fmac_f32_e32 v127, v26, v123
	v_add_f32_e32 v141, v34, v127
	v_mul_f32_e32 v128, v18, v123
	v_fmac_f32_e32 v128, v10, v122
	v_fmac_f32_e32 v128, v26, v124
	v_add_f32_e32 v142, v34, v128
	v_mul_f32_e32 v129, v18, v124
	v_fmac_f32_e32 v129, v10, v123
	v_fmac_f32_e32 v129, v26, v125
	v_add_f32_e32 v143, v34, v129
	v_and_b32_e32 v120, 0xffff0000, v73
	v_and_b32_e32 v121, 0xffff0000, v77
	v_and_b32_e32 v122, 0xffff0000, v81
	v_and_b32_e32 v123, 0xffff0000, v85
	v_and_b32_e32 v124, 0xffff0000, v89
	v_and_b32_e32 v125, 0xffff0000, v93
	v_mul_f32_e32 v126, v19, v121
	v_fmac_f32_e32 v126, v11, v120
	v_fmac_f32_e32 v126, v27, v122
	v_add_f32_e32 v144, v35, v126
	v_mul_f32_e32 v127, v19, v122
	v_fmac_f32_e32 v127, v11, v121
	v_fmac_f32_e32 v127, v27, v123
	v_add_f32_e32 v145, v35, v127
	v_mul_f32_e32 v128, v19, v123
	v_fmac_f32_e32 v128, v11, v122
	v_fmac_f32_e32 v128, v27, v124
	v_add_f32_e32 v146, v35, v128
	v_mul_f32_e32 v129, v19, v124
	v_fmac_f32_e32 v129, v11, v123
	v_fmac_f32_e32 v129, v27, v125
	v_add_f32_e32 v147, v35, v129
	v_lshlrev_b32_e32 v120, 16, v74
	v_lshlrev_b32_e32 v121, 16, v78
	v_lshlrev_b32_e32 v122, 16, v82
	v_lshlrev_b32_e32 v123, 16, v86
	v_lshlrev_b32_e32 v124, 16, v90
	v_lshlrev_b32_e32 v125, 16, v94
	v_mul_f32_e32 v126, v20, v121
	v_fmac_f32_e32 v126, v12, v120
	v_fmac_f32_e32 v126, v28, v122
	v_add_f32_e32 v148, v36, v126
	v_mul_f32_e32 v127, v20, v122
	v_fmac_f32_e32 v127, v12, v121
	v_fmac_f32_e32 v127, v28, v123
	v_add_f32_e32 v149, v36, v127
	v_mul_f32_e32 v128, v20, v123
	v_fmac_f32_e32 v128, v12, v122
	v_fmac_f32_e32 v128, v28, v124
	v_add_f32_e32 v150, v36, v128
	v_mul_f32_e32 v129, v20, v124
	v_fmac_f32_e32 v129, v12, v123
	v_fmac_f32_e32 v129, v28, v125
	v_add_f32_e32 v151, v36, v129
	v_and_b32_e32 v120, 0xffff0000, v74
	v_and_b32_e32 v121, 0xffff0000, v78
	v_and_b32_e32 v122, 0xffff0000, v82
	v_and_b32_e32 v123, 0xffff0000, v86
	v_and_b32_e32 v124, 0xffff0000, v90
	v_and_b32_e32 v125, 0xffff0000, v94
	v_mul_f32_e32 v126, v21, v121
	v_fmac_f32_e32 v126, v13, v120
	v_fmac_f32_e32 v126, v29, v122
	v_add_f32_e32 v152, v37, v126
	v_mul_f32_e32 v127, v21, v122
	v_fmac_f32_e32 v127, v13, v121
	v_fmac_f32_e32 v127, v29, v123
	v_add_f32_e32 v153, v37, v127
	v_mul_f32_e32 v128, v21, v123
	v_fmac_f32_e32 v128, v13, v122
	v_fmac_f32_e32 v128, v29, v124
	v_add_f32_e32 v154, v37, v128
	v_mul_f32_e32 v129, v21, v124
	v_fmac_f32_e32 v129, v13, v123
	v_fmac_f32_e32 v129, v29, v125
	v_add_f32_e32 v155, v37, v129
	v_lshlrev_b32_e32 v120, 16, v75
	v_lshlrev_b32_e32 v121, 16, v79
	v_lshlrev_b32_e32 v122, 16, v83
	v_lshlrev_b32_e32 v123, 16, v87
	v_lshlrev_b32_e32 v124, 16, v91
	v_lshlrev_b32_e32 v125, 16, v95
	v_mul_f32_e32 v126, v22, v121
	v_fmac_f32_e32 v126, v14, v120
	v_fmac_f32_e32 v126, v30, v122
	v_add_f32_e32 v156, v38, v126
	v_mul_f32_e32 v127, v22, v122
	v_fmac_f32_e32 v127, v14, v121
	v_fmac_f32_e32 v127, v30, v123
	v_add_f32_e32 v157, v38, v127
	v_mul_f32_e32 v128, v22, v123
	v_fmac_f32_e32 v128, v14, v122
	v_fmac_f32_e32 v128, v30, v124
	v_add_f32_e32 v158, v38, v128
	v_mul_f32_e32 v129, v22, v124
	v_fmac_f32_e32 v129, v14, v123
	v_fmac_f32_e32 v129, v30, v125
	v_add_f32_e32 v159, v38, v129
	v_and_b32_e32 v120, 0xffff0000, v75
	v_and_b32_e32 v121, 0xffff0000, v79
	v_and_b32_e32 v122, 0xffff0000, v83
	v_and_b32_e32 v123, 0xffff0000, v87
	v_and_b32_e32 v124, 0xffff0000, v91
	v_and_b32_e32 v125, 0xffff0000, v95
	v_mul_f32_e32 v126, v23, v121
	v_fmac_f32_e32 v126, v15, v120
	v_fmac_f32_e32 v126, v31, v122
	v_add_f32_e32 v160, v39, v126
	v_mul_f32_e32 v127, v23, v122
	v_fmac_f32_e32 v127, v15, v121
	v_fmac_f32_e32 v127, v31, v123
	v_add_f32_e32 v161, v39, v127
	v_mul_f32_e32 v128, v23, v123
	v_fmac_f32_e32 v128, v15, v122
	v_fmac_f32_e32 v128, v31, v124
	v_add_f32_e32 v162, v39, v128
	v_mul_f32_e32 v129, v23, v124
	v_fmac_f32_e32 v129, v15, v123
	v_fmac_f32_e32 v129, v31, v125
	v_add_f32_e32 v163, v39, v129
	v_lshlrev_b32_e32 v120, 16, v96
	v_lshlrev_b32_e32 v121, 16, v100
	v_lshlrev_b32_e32 v122, 16, v104
	v_lshlrev_b32_e32 v123, 16, v108
	v_lshlrev_b32_e32 v124, 16, v112
	v_lshlrev_b32_e32 v125, 16, v116
	v_mul_f32_e32 v126, v48, v121
	v_fmac_f32_e32 v126, v40, v120
	v_fmac_f32_e32 v126, v56, v122
	v_add_f32_e32 v126, v64, v126
	v_mul_f32_e32 v132, v132, v126
	v_mul_f32_e32 v127, v48, v122
	v_fmac_f32_e32 v127, v40, v121
	v_fmac_f32_e32 v127, v56, v123
	v_add_f32_e32 v127, v64, v127
	v_mul_f32_e32 v133, v133, v127
	v_mul_f32_e32 v128, v48, v123
	v_fmac_f32_e32 v128, v40, v122
	v_fmac_f32_e32 v128, v56, v124
	v_add_f32_e32 v128, v64, v128
	v_mul_f32_e32 v134, v134, v128
	v_mul_f32_e32 v129, v48, v124
	v_fmac_f32_e32 v129, v40, v123
	v_fmac_f32_e32 v129, v56, v125
	v_add_f32_e32 v129, v64, v129
	v_mul_f32_e32 v135, v135, v129
	v_and_b32_e32 v120, 0xffff0000, v96
	v_and_b32_e32 v121, 0xffff0000, v100
	v_and_b32_e32 v122, 0xffff0000, v104
	v_and_b32_e32 v123, 0xffff0000, v108
	v_and_b32_e32 v124, 0xffff0000, v112
	v_and_b32_e32 v125, 0xffff0000, v116
	v_mul_f32_e32 v126, v49, v121
	v_fmac_f32_e32 v126, v41, v120
	v_fmac_f32_e32 v126, v57, v122
	v_add_f32_e32 v126, v65, v126
	v_mul_f32_e32 v136, v136, v126
	v_mul_f32_e32 v127, v49, v122
	v_fmac_f32_e32 v127, v41, v121
	v_fmac_f32_e32 v127, v57, v123
	v_add_f32_e32 v127, v65, v127
	v_mul_f32_e32 v137, v137, v127
	v_mul_f32_e32 v128, v49, v123
	v_fmac_f32_e32 v128, v41, v122
	v_fmac_f32_e32 v128, v57, v124
	v_add_f32_e32 v128, v65, v128
	v_mul_f32_e32 v138, v138, v128
	v_mul_f32_e32 v129, v49, v124
	v_fmac_f32_e32 v129, v41, v123
	v_fmac_f32_e32 v129, v57, v125
	v_add_f32_e32 v129, v65, v129
	v_mul_f32_e32 v139, v139, v129
	v_lshlrev_b32_e32 v120, 16, v97
	v_lshlrev_b32_e32 v121, 16, v101
	v_lshlrev_b32_e32 v122, 16, v105
	v_lshlrev_b32_e32 v123, 16, v109
	v_lshlrev_b32_e32 v124, 16, v113
	v_lshlrev_b32_e32 v125, 16, v117
	v_mul_f32_e32 v126, v50, v121
	v_fmac_f32_e32 v126, v42, v120
	v_fmac_f32_e32 v126, v58, v122
	v_add_f32_e32 v126, v66, v126
	v_mul_f32_e32 v140, v140, v126
	v_mul_f32_e32 v127, v50, v122
	v_fmac_f32_e32 v127, v42, v121
	v_fmac_f32_e32 v127, v58, v123
	v_add_f32_e32 v127, v66, v127
	v_mul_f32_e32 v141, v141, v127
	v_mul_f32_e32 v128, v50, v123
	v_fmac_f32_e32 v128, v42, v122
	v_fmac_f32_e32 v128, v58, v124
	v_add_f32_e32 v128, v66, v128
	v_mul_f32_e32 v142, v142, v128
	v_mul_f32_e32 v129, v50, v124
	v_fmac_f32_e32 v129, v42, v123
	v_fmac_f32_e32 v129, v58, v125
	v_add_f32_e32 v129, v66, v129
	v_mul_f32_e32 v143, v143, v129
	v_and_b32_e32 v120, 0xffff0000, v97
	v_and_b32_e32 v121, 0xffff0000, v101
	v_and_b32_e32 v122, 0xffff0000, v105
	v_and_b32_e32 v123, 0xffff0000, v109
	v_and_b32_e32 v124, 0xffff0000, v113
	v_and_b32_e32 v125, 0xffff0000, v117
	v_mul_f32_e32 v126, v51, v121
	v_fmac_f32_e32 v126, v43, v120
	v_fmac_f32_e32 v126, v59, v122
	v_add_f32_e32 v126, v67, v126
	v_mul_f32_e32 v144, v144, v126
	v_mul_f32_e32 v127, v51, v122
	v_fmac_f32_e32 v127, v43, v121
	v_fmac_f32_e32 v127, v59, v123
	v_add_f32_e32 v127, v67, v127
	v_mul_f32_e32 v145, v145, v127
	v_mul_f32_e32 v128, v51, v123
	v_fmac_f32_e32 v128, v43, v122
	v_fmac_f32_e32 v128, v59, v124
	v_add_f32_e32 v128, v67, v128
	v_mul_f32_e32 v146, v146, v128
	v_mul_f32_e32 v129, v51, v124
	v_fmac_f32_e32 v129, v43, v123
	v_fmac_f32_e32 v129, v59, v125
	v_add_f32_e32 v129, v67, v129
	v_mul_f32_e32 v147, v147, v129
	v_lshlrev_b32_e32 v120, 16, v98
	v_lshlrev_b32_e32 v121, 16, v102
	v_lshlrev_b32_e32 v122, 16, v106
	v_lshlrev_b32_e32 v123, 16, v110
	v_lshlrev_b32_e32 v124, 16, v114
	v_lshlrev_b32_e32 v125, 16, v118
	v_mul_f32_e32 v126, v52, v121
	v_fmac_f32_e32 v126, v44, v120
	v_fmac_f32_e32 v126, v60, v122
	v_add_f32_e32 v126, v68, v126
	v_mul_f32_e32 v148, v148, v126
	v_mul_f32_e32 v127, v52, v122
	v_fmac_f32_e32 v127, v44, v121
	v_fmac_f32_e32 v127, v60, v123
	v_add_f32_e32 v127, v68, v127
	v_mul_f32_e32 v149, v149, v127
	v_mul_f32_e32 v128, v52, v123
	v_fmac_f32_e32 v128, v44, v122
	v_fmac_f32_e32 v128, v60, v124
	v_add_f32_e32 v128, v68, v128
	v_mul_f32_e32 v150, v150, v128
	v_mul_f32_e32 v129, v52, v124
	v_fmac_f32_e32 v129, v44, v123
	v_fmac_f32_e32 v129, v60, v125
	v_add_f32_e32 v129, v68, v129
	v_mul_f32_e32 v151, v151, v129
	v_and_b32_e32 v120, 0xffff0000, v98
	v_and_b32_e32 v121, 0xffff0000, v102
	v_and_b32_e32 v122, 0xffff0000, v106
	v_and_b32_e32 v123, 0xffff0000, v110
	v_and_b32_e32 v124, 0xffff0000, v114
	v_and_b32_e32 v125, 0xffff0000, v118
	v_mul_f32_e32 v126, v53, v121
	v_fmac_f32_e32 v126, v45, v120
	v_fmac_f32_e32 v126, v61, v122
	v_add_f32_e32 v126, v69, v126
	v_mul_f32_e32 v152, v152, v126
	v_mul_f32_e32 v127, v53, v122
	v_fmac_f32_e32 v127, v45, v121
	v_fmac_f32_e32 v127, v61, v123
	v_add_f32_e32 v127, v69, v127
	v_mul_f32_e32 v153, v153, v127
	v_mul_f32_e32 v128, v53, v123
	v_fmac_f32_e32 v128, v45, v122
	v_fmac_f32_e32 v128, v61, v124
	v_add_f32_e32 v128, v69, v128
	v_mul_f32_e32 v154, v154, v128
	v_mul_f32_e32 v129, v53, v124
	v_fmac_f32_e32 v129, v45, v123
	v_fmac_f32_e32 v129, v61, v125
	v_add_f32_e32 v129, v69, v129
	v_mul_f32_e32 v155, v155, v129
	v_lshlrev_b32_e32 v120, 16, v99
	v_lshlrev_b32_e32 v121, 16, v103
	v_lshlrev_b32_e32 v122, 16, v107
	v_lshlrev_b32_e32 v123, 16, v111
	v_lshlrev_b32_e32 v124, 16, v115
	v_lshlrev_b32_e32 v125, 16, v119
	v_mul_f32_e32 v126, v54, v121
	v_fmac_f32_e32 v126, v46, v120
	v_fmac_f32_e32 v126, v62, v122
	v_add_f32_e32 v126, v70, v126
	v_mul_f32_e32 v156, v156, v126
	v_mul_f32_e32 v127, v54, v122
	v_fmac_f32_e32 v127, v46, v121
	v_fmac_f32_e32 v127, v62, v123
	v_add_f32_e32 v127, v70, v127
	v_mul_f32_e32 v157, v157, v127
	v_mul_f32_e32 v128, v54, v123
	v_fmac_f32_e32 v128, v46, v122
	v_fmac_f32_e32 v128, v62, v124
	v_add_f32_e32 v128, v70, v128
	v_mul_f32_e32 v158, v158, v128
	v_mul_f32_e32 v129, v54, v124
	v_fmac_f32_e32 v129, v46, v123
	v_fmac_f32_e32 v129, v62, v125
	v_add_f32_e32 v129, v70, v129
	v_mul_f32_e32 v159, v159, v129
	v_and_b32_e32 v120, 0xffff0000, v99
	v_and_b32_e32 v121, 0xffff0000, v103
	v_and_b32_e32 v122, 0xffff0000, v107
	v_and_b32_e32 v123, 0xffff0000, v111
	v_and_b32_e32 v124, 0xffff0000, v115
	v_and_b32_e32 v125, 0xffff0000, v119
	v_mul_f32_e32 v126, v55, v121
	v_fmac_f32_e32 v126, v47, v120
	v_fmac_f32_e32 v126, v63, v122
	v_add_f32_e32 v126, v71, v126
	v_mul_f32_e32 v160, v160, v126
	v_mul_f32_e32 v127, v55, v122
	v_fmac_f32_e32 v127, v47, v121
	v_fmac_f32_e32 v127, v63, v123
	v_add_f32_e32 v127, v71, v127
	v_mul_f32_e32 v161, v161, v127
	v_mul_f32_e32 v128, v55, v123
	v_fmac_f32_e32 v128, v47, v122
	v_fmac_f32_e32 v128, v63, v124
	v_add_f32_e32 v128, v71, v128
	v_mul_f32_e32 v162, v162, v128
	v_mul_f32_e32 v129, v55, v124
	v_fmac_f32_e32 v129, v47, v123
	v_fmac_f32_e32 v129, v63, v125
	v_add_f32_e32 v129, v71, v129
	v_mul_f32_e32 v163, v163, v129
	s_lshr_b32 s16, s12, 2
	s_lshl_b32 s16, s16, 8
	s_lshl_b32 s17, s14, 16
	s_add_u32 s16, s16, s17
	s_add_u32 s24, s6, s16
	s_addc_u32 s25, s7, 0
	s_add_i32 s12, s12, s62
	s_cmp_lt_i32 s12, s20
	s_cbranch_scc0 .Luin_nonext
	s_lshr_b32 s13, s12, 2
	s_lshl_b32 s13, s13, 6
	v_lshl_add_u32 v3, v2, 2, s13
	v_add_u32_e32 v4, 4, v3
	v_add_u32_e32 v3, -1, v3
	v_mul_lo_u32 v165, v3, s26
	v_lshl_add_u32 v126, v1, 4, s15
	v_add_u32_e32 v165, v165, v126
	v_add_u32_e32 v166, 0x3200, v165
	v_add_u32_e32 v167, 0x3200, v166
	v_add_u32_e32 v168, 0x3200, v167
	v_add_u32_e32 v169, 0x3200, v168
	v_add_u32_e32 v170, 0x3200, v169
	v_mov_b32_e32 v72, 0
	v_mov_b32_e32 v73, 0
	v_mov_b32_e32 v74, 0
	v_mov_b32_e32 v75, 0
	v_mov_b32_e32 v92, 0
	v_mov_b32_e32 v93, 0
	v_mov_b32_e32 v94, 0
	v_mov_b32_e32 v95, 0
	v_mov_b32_e32 v96, 0
	v_mov_b32_e32 v97, 0
	v_mov_b32_e32 v98, 0
	v_mov_b32_e32 v99, 0
	v_mov_b32_e32 v116, 0
	v_mov_b32_e32 v117, 0
	v_mov_b32_e32 v118, 0
	v_mov_b32_e32 v119, 0
	global_load_dwordx4 v[76:79], v166, s[4:5]
	global_load_dwordx4 v[100:103], v166, s[4:5] offset:2048
	global_load_dwordx4 v[80:83], v167, s[4:5]
	global_load_dwordx4 v[104:107], v167, s[4:5] offset:2048
	global_load_dwordx4 v[84:87], v168, s[4:5]
	global_load_dwordx4 v[108:111], v168, s[4:5] offset:2048
	global_load_dwordx4 v[88:91], v169, s[4:5]
	global_load_dwordx4 v[112:115], v169, s[4:5] offset:2048
	v_cmp_le_i32_e32 vcc, 0, v3
	s_and_saveexec_b64 s[22:23], vcc
	global_load_dwordx4 v[72:75], v165, s[4:5]
	global_load_dwordx4 v[96:99], v165, s[4:5] offset:2048
	s_mov_b64 exec, s[22:23]
	v_cmp_gt_i32_e32 vcc, s27, v4
	s_and_saveexec_b64 s[22:23], vcc
	global_load_dwordx4 v[92:95], v170, s[4:5]
	global_load_dwordx4 v[116:119], v170, s[4:5] offset:2048
	s_mov_b64 exec, s[22:23]
.Luin_nonext:
	ds_write_b128 v6, v[132:135]
	ds_write_b128 v6, v[136:139] offset:272
	ds_write_b128 v6, v[140:143] offset:544
	ds_write_b128 v6, v[144:147] offset:816
	ds_write_b128 v6, v[148:151] offset:1088
	ds_write_b128 v6, v[152:155] offset:1360
	ds_write_b128 v6, v[156:159] offset:1632
	ds_write_b128 v6, v[160:163] offset:1904
	s_waitcnt lgkmcnt(0)
	s_barrier
	ds_read_b128 v[172:175], v7
	s_waitcnt lgkmcnt(0)
	global_store_dwordx4 v164, v[172:175], s[24:25]
	s_nop 1
	s_add_u32 s24, s24, 0x200000
	s_addc_u32 s25, s25, 0
	ds_read_b128 v[172:175], v7 offset:8704
	s_waitcnt lgkmcnt(0)
	global_store_dwordx4 v164, v[172:175], s[24:25]
	s_nop 1
	s_add_u32 s24, s24, 0x200000
	s_addc_u32 s25, s25, 0
	ds_read_b128 v[172:175], v7 offset:17408
	s_waitcnt lgkmcnt(0)
	global_store_dwordx4 v164, v[172:175], s[24:25]
	s_nop 1
	s_add_u32 s24, s24, 0x200000
	s_addc_u32 s25, s25, 0
	ds_read_b128 v[172:175], v7 offset:26112
	s_waitcnt lgkmcnt(0)
	global_store_dwordx4 v164, v[172:175], s[24:25]
	s_nop 1
	s_add_u32 s24, s24, 0x200000
	s_addc_u32 s25, s25, 0
	ds_read_b128 v[172:175], v7 offset:34816
	s_waitcnt lgkmcnt(0)
	global_store_dwordx4 v164, v[172:175], s[24:25]
	s_nop 1
	s_add_u32 s24, s24, 0x200000
	s_addc_u32 s25, s25, 0
	ds_read_b128 v[172:175], v7 offset:43520
	s_waitcnt lgkmcnt(0)
	global_store_dwordx4 v164, v[172:175], s[24:25]
	s_nop 1
	s_add_u32 s24, s24, 0x200000
	s_addc_u32 s25, s25, 0
	ds_read_b128 v[172:175], v7 offset:52224
	s_waitcnt lgkmcnt(0)
	global_store_dwordx4 v164, v[172:175], s[24:25]
	s_nop 1
	s_add_u32 s24, s24, 0x200000
	s_addc_u32 s25, s25, 0
	ds_read_b128 v[172:175], v7 offset:60928
	s_waitcnt lgkmcnt(0)
	global_store_dwordx4 v164, v[172:175], s[24:25]
	s_nop 1
	s_barrier
	s_cmp_lt_i32 s12, s20
	s_cbranch_scc1 .Luin_tile
	s_cmp_eq_u32 s21, 0
	s_cbranch_scc1 .LBB0_506
	s_sub_u32 s28, s92, 16
	s_lshr_b32 s29, s28, 2
	s_and_b32 s30, s29, 3
	s_lshr_b32 s29, s29, 2
	s_lshl_b32 s29, s29, 2
	s_and_b32 s31, s92, 3
	s_or_b32 s29, s29, s31
	s_add_u32 s12, s29, 0x300
	v_readfirstlane_b32 s31, v0
	s_lshr_b32 s31, s31, 7
	s_cmp_lg_u32 s31, s30
	s_cbranch_scc1 .Luin_qskip
	s_lshr_b32 s13, s12, 2
	s_lshl_b32 s13, s13, 6
	v_lshl_add_u32 v3, v2, 2, s13
	v_add_u32_e32 v4, 4, v3
	v_add_u32_e32 v3, -1, v3
	v_mul_lo_u32 v165, v3, s26
	v_lshl_add_u32 v126, v1, 4, s15
	v_add_u32_e32 v165, v165, v126
	v_add_u32_e32 v166, 0x3200, v165
	v_add_u32_e32 v167, 0x3200, v166
	v_add_u32_e32 v168, 0x3200, v167
	v_add_u32_e32 v169, 0x3200, v168
	v_add_u32_e32 v170, 0x3200, v169
	v_mov_b32_e32 v72, 0
	v_mov_b32_e32 v73, 0
	v_mov_b32_e32 v74, 0
	v_mov_b32_e32 v75, 0
	v_mov_b32_e32 v92, 0
	v_mov_b32_e32 v93, 0
	v_mov_b32_e32 v94, 0
	v_mov_b32_e32 v95, 0
	v_mov_b32_e32 v96, 0
	v_mov_b32_e32 v97, 0
	v_mov_b32_e32 v98, 0
	v_mov_b32_e32 v99, 0
	v_mov_b32_e32 v116, 0
	v_mov_b32_e32 v117, 0
	v_mov_b32_e32 v118, 0
	v_mov_b32_e32 v119, 0
	global_load_dwordx4 v[76:79], v166, s[4:5]
	global_load_dwordx4 v[100:103], v166, s[4:5] offset:2048
	global_load_dwordx4 v[80:83], v167, s[4:5]
	global_load_dwordx4 v[104:107], v167, s[4:5] offset:2048
	global_load_dwordx4 v[84:87], v168, s[4:5]
	global_load_dwordx4 v[108:111], v168, s[4:5] offset:2048
	global_load_dwordx4 v[88:91], v169, s[4:5]
	global_load_dwordx4 v[112:115], v169, s[4:5] offset:2048
	v_cmp_le_i32_e32 vcc, 0, v3
	s_and_saveexec_b64 s[22:23], vcc
	global_load_dwordx4 v[72:75], v165, s[4:5]
	global_load_dwordx4 v[96:99], v165, s[4:5] offset:2048
	s_mov_b64 exec, s[22:23]
	v_cmp_gt_i32_e32 vcc, s27, v4
	s_and_saveexec_b64 s[22:23], vcc
	global_load_dwordx4 v[92:95], v170, s[4:5]
	global_load_dwordx4 v[116:119], v170, s[4:5] offset:2048
	s_mov_b64 exec, s[22:23]
	s_waitcnt vmcnt(0)
	v_lshlrev_b32_e32 v120, 16, v72
	v_lshlrev_b32_e32 v121, 16, v76
	v_lshlrev_b32_e32 v122, 16, v80
	v_lshlrev_b32_e32 v123, 16, v84
	v_lshlrev_b32_e32 v124, 16, v88
	v_lshlrev_b32_e32 v125, 16, v92
	v_mul_f32_e32 v126, v16, v121
	v_fmac_f32_e32 v126, v8, v120
	v_fmac_f32_e32 v126, v24, v122
	v_add_f32_e32 v132, v32, v126
	v_mul_f32_e32 v127, v16, v122
	v_fmac_f32_e32 v127, v8, v121
	v_fmac_f32_e32 v127, v24, v123
	v_add_f32_e32 v133, v32, v127
	v_mul_f32_e32 v128, v16, v123
	v_fmac_f32_e32 v128, v8, v122
	v_fmac_f32_e32 v128, v24, v124
	v_add_f32_e32 v134, v32, v128
	v_mul_f32_e32 v129, v16, v124
	v_fmac_f32_e32 v129, v8, v123
	v_fmac_f32_e32 v129, v24, v125
	v_add_f32_e32 v135, v32, v129
	v_and_b32_e32 v120, 0xffff0000, v72
	v_and_b32_e32 v121, 0xffff0000, v76
	v_and_b32_e32 v122, 0xffff0000, v80
	v_and_b32_e32 v123, 0xffff0000, v84
	v_and_b32_e32 v124, 0xffff0000, v88
	v_and_b32_e32 v125, 0xffff0000, v92
	v_mul_f32_e32 v126, v17, v121
	v_fmac_f32_e32 v126, v9, v120
	v_fmac_f32_e32 v126, v25, v122
	v_add_f32_e32 v136, v33, v126
	v_mul_f32_e32 v127, v17, v122
	v_fmac_f32_e32 v127, v9, v121
	v_fmac_f32_e32 v127, v25, v123
	v_add_f32_e32 v137, v33, v127
	v_mul_f32_e32 v128, v17, v123
	v_fmac_f32_e32 v128, v9, v122
	v_fmac_f32_e32 v128, v25, v124
	v_add_f32_e32 v138, v33, v128
	v_mul_f32_e32 v129, v17, v124
	v_fmac_f32_e32 v129, v9, v123
	v_fmac_f32_e32 v129, v25, v125
	v_add_f32_e32 v139, v33, v129
	v_lshlrev_b32_e32 v120, 16, v73
	v_lshlrev_b32_e32 v121, 16, v77
	v_lshlrev_b32_e32 v122, 16, v81
	v_lshlrev_b32_e32 v123, 16, v85
	v_lshlrev_b32_e32 v124, 16, v89
	v_lshlrev_b32_e32 v125, 16, v93
	v_mul_f32_e32 v126, v18, v121
	v_fmac_f32_e32 v126, v10, v120
	v_fmac_f32_e32 v126, v26, v122
	v_add_f32_e32 v140, v34, v126
	v_mul_f32_e32 v127, v18, v122
	v_fmac_f32_e32 v127, v10, v121
	v_fmac_f32_e32 v127, v26, v123
	v_add_f32_e32 v141, v34, v127
	v_mul_f32_e32 v128, v18, v123
	v_fmac_f32_e32 v128, v10, v122
	v_fmac_f32_e32 v128, v26, v124
	v_add_f32_e32 v142, v34, v128
	v_mul_f32_e32 v129, v18, v124
	v_fmac_f32_e32 v129, v10, v123
	v_fmac_f32_e32 v129, v26, v125
	v_add_f32_e32 v143, v34, v129
	v_and_b32_e32 v120, 0xffff0000, v73
	v_and_b32_e32 v121, 0xffff0000, v77
	v_and_b32_e32 v122, 0xffff0000, v81
	v_and_b32_e32 v123, 0xffff0000, v85
	v_and_b32_e32 v124, 0xffff0000, v89
	v_and_b32_e32 v125, 0xffff0000, v93
	v_mul_f32_e32 v126, v19, v121
	v_fmac_f32_e32 v126, v11, v120
	v_fmac_f32_e32 v126, v27, v122
	v_add_f32_e32 v144, v35, v126
	v_mul_f32_e32 v127, v19, v122
	v_fmac_f32_e32 v127, v11, v121
	v_fmac_f32_e32 v127, v27, v123
	v_add_f32_e32 v145, v35, v127
	v_mul_f32_e32 v128, v19, v123
	v_fmac_f32_e32 v128, v11, v122
	v_fmac_f32_e32 v128, v27, v124
	v_add_f32_e32 v146, v35, v128
	v_mul_f32_e32 v129, v19, v124
	v_fmac_f32_e32 v129, v11, v123
	v_fmac_f32_e32 v129, v27, v125
	v_add_f32_e32 v147, v35, v129
	v_lshlrev_b32_e32 v120, 16, v74
	v_lshlrev_b32_e32 v121, 16, v78
	v_lshlrev_b32_e32 v122, 16, v82
	v_lshlrev_b32_e32 v123, 16, v86
	v_lshlrev_b32_e32 v124, 16, v90
	v_lshlrev_b32_e32 v125, 16, v94
	v_mul_f32_e32 v126, v20, v121
	v_fmac_f32_e32 v126, v12, v120
	v_fmac_f32_e32 v126, v28, v122
	v_add_f32_e32 v148, v36, v126
	v_mul_f32_e32 v127, v20, v122
	v_fmac_f32_e32 v127, v12, v121
	v_fmac_f32_e32 v127, v28, v123
	v_add_f32_e32 v149, v36, v127
	v_mul_f32_e32 v128, v20, v123
	v_fmac_f32_e32 v128, v12, v122
	v_fmac_f32_e32 v128, v28, v124
	v_add_f32_e32 v150, v36, v128
	v_mul_f32_e32 v129, v20, v124
	v_fmac_f32_e32 v129, v12, v123
	v_fmac_f32_e32 v129, v28, v125
	v_add_f32_e32 v151, v36, v129
	v_and_b32_e32 v120, 0xffff0000, v74
	v_and_b32_e32 v121, 0xffff0000, v78
	v_and_b32_e32 v122, 0xffff0000, v82
	v_and_b32_e32 v123, 0xffff0000, v86
	v_and_b32_e32 v124, 0xffff0000, v90
	v_and_b32_e32 v125, 0xffff0000, v94
	v_mul_f32_e32 v126, v21, v121
	v_fmac_f32_e32 v126, v13, v120
	v_fmac_f32_e32 v126, v29, v122
	v_add_f32_e32 v152, v37, v126
	v_mul_f32_e32 v127, v21, v122
	v_fmac_f32_e32 v127, v13, v121
	v_fmac_f32_e32 v127, v29, v123
	v_add_f32_e32 v153, v37, v127
	v_mul_f32_e32 v128, v21, v123
	v_fmac_f32_e32 v128, v13, v122
	v_fmac_f32_e32 v128, v29, v124
	v_add_f32_e32 v154, v37, v128
	v_mul_f32_e32 v129, v21, v124
	v_fmac_f32_e32 v129, v13, v123
	v_fmac_f32_e32 v129, v29, v125
	v_add_f32_e32 v155, v37, v129
	v_lshlrev_b32_e32 v120, 16, v75
	v_lshlrev_b32_e32 v121, 16, v79
	v_lshlrev_b32_e32 v122, 16, v83
	v_lshlrev_b32_e32 v123, 16, v87
	v_lshlrev_b32_e32 v124, 16, v91
	v_lshlrev_b32_e32 v125, 16, v95
	v_mul_f32_e32 v126, v22, v121
	v_fmac_f32_e32 v126, v14, v120
	v_fmac_f32_e32 v126, v30, v122
	v_add_f32_e32 v156, v38, v126
	v_mul_f32_e32 v127, v22, v122
	v_fmac_f32_e32 v127, v14, v121
	v_fmac_f32_e32 v127, v30, v123
	v_add_f32_e32 v157, v38, v127
	v_mul_f32_e32 v128, v22, v123
	v_fmac_f32_e32 v128, v14, v122
	v_fmac_f32_e32 v128, v30, v124
	v_add_f32_e32 v158, v38, v128
	v_mul_f32_e32 v129, v22, v124
	v_fmac_f32_e32 v129, v14, v123
	v_fmac_f32_e32 v129, v30, v125
	v_add_f32_e32 v159, v38, v129
	v_and_b32_e32 v120, 0xffff0000, v75
	v_and_b32_e32 v121, 0xffff0000, v79
	v_and_b32_e32 v122, 0xffff0000, v83
	v_and_b32_e32 v123, 0xffff0000, v87
	v_and_b32_e32 v124, 0xffff0000, v91
	v_and_b32_e32 v125, 0xffff0000, v95
	v_mul_f32_e32 v126, v23, v121
	v_fmac_f32_e32 v126, v15, v120
	v_fmac_f32_e32 v126, v31, v122
	v_add_f32_e32 v160, v39, v126
	v_mul_f32_e32 v127, v23, v122
	v_fmac_f32_e32 v127, v15, v121
	v_fmac_f32_e32 v127, v31, v123
	v_add_f32_e32 v161, v39, v127
	v_mul_f32_e32 v128, v23, v123
	v_fmac_f32_e32 v128, v15, v122
	v_fmac_f32_e32 v128, v31, v124
	v_add_f32_e32 v162, v39, v128
	v_mul_f32_e32 v129, v23, v124
	v_fmac_f32_e32 v129, v15, v123
	v_fmac_f32_e32 v129, v31, v125
	v_add_f32_e32 v163, v39, v129
	v_lshlrev_b32_e32 v120, 16, v96
	v_lshlrev_b32_e32 v121, 16, v100
	v_lshlrev_b32_e32 v122, 16, v104
	v_lshlrev_b32_e32 v123, 16, v108
	v_lshlrev_b32_e32 v124, 16, v112
	v_lshlrev_b32_e32 v125, 16, v116
	v_mul_f32_e32 v126, v48, v121
	v_fmac_f32_e32 v126, v40, v120
	v_fmac_f32_e32 v126, v56, v122
	v_add_f32_e32 v126, v64, v126
	v_mul_f32_e32 v132, v132, v126
	v_mul_f32_e32 v127, v48, v122
	v_fmac_f32_e32 v127, v40, v121
	v_fmac_f32_e32 v127, v56, v123
	v_add_f32_e32 v127, v64, v127
	v_mul_f32_e32 v133, v133, v127
	v_mul_f32_e32 v128, v48, v123
	v_fmac_f32_e32 v128, v40, v122
	v_fmac_f32_e32 v128, v56, v124
	v_add_f32_e32 v128, v64, v128
	v_mul_f32_e32 v134, v134, v128
	v_mul_f32_e32 v129, v48, v124
	v_fmac_f32_e32 v129, v40, v123
	v_fmac_f32_e32 v129, v56, v125
	v_add_f32_e32 v129, v64, v129
	v_mul_f32_e32 v135, v135, v129
	v_and_b32_e32 v120, 0xffff0000, v96
	v_and_b32_e32 v121, 0xffff0000, v100
	v_and_b32_e32 v122, 0xffff0000, v104
	v_and_b32_e32 v123, 0xffff0000, v108
	v_and_b32_e32 v124, 0xffff0000, v112
	v_and_b32_e32 v125, 0xffff0000, v116
	v_mul_f32_e32 v126, v49, v121
	v_fmac_f32_e32 v126, v41, v120
	v_fmac_f32_e32 v126, v57, v122
	v_add_f32_e32 v126, v65, v126
	v_mul_f32_e32 v136, v136, v126
	v_mul_f32_e32 v127, v49, v122
	v_fmac_f32_e32 v127, v41, v121
	v_fmac_f32_e32 v127, v57, v123
	v_add_f32_e32 v127, v65, v127
	v_mul_f32_e32 v137, v137, v127
	v_mul_f32_e32 v128, v49, v123
	v_fmac_f32_e32 v128, v41, v122
	v_fmac_f32_e32 v128, v57, v124
	v_add_f32_e32 v128, v65, v128
	v_mul_f32_e32 v138, v138, v128
	v_mul_f32_e32 v129, v49, v124
	v_fmac_f32_e32 v129, v41, v123
	v_fmac_f32_e32 v129, v57, v125
	v_add_f32_e32 v129, v65, v129
	v_mul_f32_e32 v139, v139, v129
	v_lshlrev_b32_e32 v120, 16, v97
	v_lshlrev_b32_e32 v121, 16, v101
	v_lshlrev_b32_e32 v122, 16, v105
	v_lshlrev_b32_e32 v123, 16, v109
	v_lshlrev_b32_e32 v124, 16, v113
	v_lshlrev_b32_e32 v125, 16, v117
	v_mul_f32_e32 v126, v50, v121
	v_fmac_f32_e32 v126, v42, v120
	v_fmac_f32_e32 v126, v58, v122
	v_add_f32_e32 v126, v66, v126
	v_mul_f32_e32 v140, v140, v126
	v_mul_f32_e32 v127, v50, v122
	v_fmac_f32_e32 v127, v42, v121
	v_fmac_f32_e32 v127, v58, v123
	v_add_f32_e32 v127, v66, v127
	v_mul_f32_e32 v141, v141, v127
	v_mul_f32_e32 v128, v50, v123
	v_fmac_f32_e32 v128, v42, v122
	v_fmac_f32_e32 v128, v58, v124
	v_add_f32_e32 v128, v66, v128
	v_mul_f32_e32 v142, v142, v128
	v_mul_f32_e32 v129, v50, v124
	v_fmac_f32_e32 v129, v42, v123
	v_fmac_f32_e32 v129, v58, v125
	v_add_f32_e32 v129, v66, v129
	v_mul_f32_e32 v143, v143, v129
	v_and_b32_e32 v120, 0xffff0000, v97
	v_and_b32_e32 v121, 0xffff0000, v101
	v_and_b32_e32 v122, 0xffff0000, v105
	v_and_b32_e32 v123, 0xffff0000, v109
	v_and_b32_e32 v124, 0xffff0000, v113
	v_and_b32_e32 v125, 0xffff0000, v117
	v_mul_f32_e32 v126, v51, v121
	v_fmac_f32_e32 v126, v43, v120
	v_fmac_f32_e32 v126, v59, v122
	v_add_f32_e32 v126, v67, v126
	v_mul_f32_e32 v144, v144, v126
	v_mul_f32_e32 v127, v51, v122
	v_fmac_f32_e32 v127, v43, v121
	v_fmac_f32_e32 v127, v59, v123
	v_add_f32_e32 v127, v67, v127
	v_mul_f32_e32 v145, v145, v127
	v_mul_f32_e32 v128, v51, v123
	v_fmac_f32_e32 v128, v43, v122
	v_fmac_f32_e32 v128, v59, v124
	v_add_f32_e32 v128, v67, v128
	v_mul_f32_e32 v146, v146, v128
	v_mul_f32_e32 v129, v51, v124
	v_fmac_f32_e32 v129, v43, v123
	v_fmac_f32_e32 v129, v59, v125
	v_add_f32_e32 v129, v67, v129
	v_mul_f32_e32 v147, v147, v129
	v_lshlrev_b32_e32 v120, 16, v98
	v_lshlrev_b32_e32 v121, 16, v102
	v_lshlrev_b32_e32 v122, 16, v106
	v_lshlrev_b32_e32 v123, 16, v110
	v_lshlrev_b32_e32 v124, 16, v114
	v_lshlrev_b32_e32 v125, 16, v118
	v_mul_f32_e32 v126, v52, v121
	v_fmac_f32_e32 v126, v44, v120
	v_fmac_f32_e32 v126, v60, v122
	v_add_f32_e32 v126, v68, v126
	v_mul_f32_e32 v148, v148, v126
	v_mul_f32_e32 v127, v52, v122
	v_fmac_f32_e32 v127, v44, v121
	v_fmac_f32_e32 v127, v60, v123
	v_add_f32_e32 v127, v68, v127
	v_mul_f32_e32 v149, v149, v127
	v_mul_f32_e32 v128, v52, v123
	v_fmac_f32_e32 v128, v44, v122
	v_fmac_f32_e32 v128, v60, v124
	v_add_f32_e32 v128, v68, v128
	v_mul_f32_e32 v150, v150, v128
	v_mul_f32_e32 v129, v52, v124
	v_fmac_f32_e32 v129, v44, v123
	v_fmac_f32_e32 v129, v60, v125
	v_add_f32_e32 v129, v68, v129
	v_mul_f32_e32 v151, v151, v129
	v_and_b32_e32 v120, 0xffff0000, v98
	v_and_b32_e32 v121, 0xffff0000, v102
	v_and_b32_e32 v122, 0xffff0000, v106
	v_and_b32_e32 v123, 0xffff0000, v110
	v_and_b32_e32 v124, 0xffff0000, v114
	v_and_b32_e32 v125, 0xffff0000, v118
	v_mul_f32_e32 v126, v53, v121
	v_fmac_f32_e32 v126, v45, v120
	v_fmac_f32_e32 v126, v61, v122
	v_add_f32_e32 v126, v69, v126
	v_mul_f32_e32 v152, v152, v126
	v_mul_f32_e32 v127, v53, v122
	v_fmac_f32_e32 v127, v45, v121
	v_fmac_f32_e32 v127, v61, v123
	v_add_f32_e32 v127, v69, v127
	v_mul_f32_e32 v153, v153, v127
	v_mul_f32_e32 v128, v53, v123
	v_fmac_f32_e32 v128, v45, v122
	v_fmac_f32_e32 v128, v61, v124
	v_add_f32_e32 v128, v69, v128
	v_mul_f32_e32 v154, v154, v128
	v_mul_f32_e32 v129, v53, v124
	v_fmac_f32_e32 v129, v45, v123
	v_fmac_f32_e32 v129, v61, v125
	v_add_f32_e32 v129, v69, v129
	v_mul_f32_e32 v155, v155, v129
	v_lshlrev_b32_e32 v120, 16, v99
	v_lshlrev_b32_e32 v121, 16, v103
	v_lshlrev_b32_e32 v122, 16, v107
	v_lshlrev_b32_e32 v123, 16, v111
	v_lshlrev_b32_e32 v124, 16, v115
	v_lshlrev_b32_e32 v125, 16, v119
	v_mul_f32_e32 v126, v54, v121
	v_fmac_f32_e32 v126, v46, v120
	v_fmac_f32_e32 v126, v62, v122
	v_add_f32_e32 v126, v70, v126
	v_mul_f32_e32 v156, v156, v126
	v_mul_f32_e32 v127, v54, v122
	v_fmac_f32_e32 v127, v46, v121
	v_fmac_f32_e32 v127, v62, v123
	v_add_f32_e32 v127, v70, v127
	v_mul_f32_e32 v157, v157, v127
	v_mul_f32_e32 v128, v54, v123
	v_fmac_f32_e32 v128, v46, v122
	v_fmac_f32_e32 v128, v62, v124
	v_add_f32_e32 v128, v70, v128
	v_mul_f32_e32 v158, v158, v128
	v_mul_f32_e32 v129, v54, v124
	v_fmac_f32_e32 v129, v46, v123
	v_fmac_f32_e32 v129, v62, v125
	v_add_f32_e32 v129, v70, v129
	v_mul_f32_e32 v159, v159, v129
	v_and_b32_e32 v120, 0xffff0000, v99
	v_and_b32_e32 v121, 0xffff0000, v103
	v_and_b32_e32 v122, 0xffff0000, v107
	v_and_b32_e32 v123, 0xffff0000, v111
	v_and_b32_e32 v124, 0xffff0000, v115
	v_and_b32_e32 v125, 0xffff0000, v119
	v_mul_f32_e32 v126, v55, v121
	v_fmac_f32_e32 v126, v47, v120
	v_fmac_f32_e32 v126, v63, v122
	v_add_f32_e32 v126, v71, v126
	v_mul_f32_e32 v160, v160, v126
	v_mul_f32_e32 v127, v55, v122
	v_fmac_f32_e32 v127, v47, v121
	v_fmac_f32_e32 v127, v63, v123
	v_add_f32_e32 v127, v71, v127
	v_mul_f32_e32 v161, v161, v127
	v_mul_f32_e32 v128, v55, v123
	v_fmac_f32_e32 v128, v47, v122
	v_fmac_f32_e32 v128, v63, v124
	v_add_f32_e32 v128, v71, v128
	v_mul_f32_e32 v162, v162, v128
	v_mul_f32_e32 v129, v55, v124
	v_fmac_f32_e32 v129, v47, v123
	v_fmac_f32_e32 v129, v63, v125
	v_add_f32_e32 v129, v71, v129
	v_mul_f32_e32 v163, v163, v129
	ds_write_b128 v6, v[132:135]
	ds_write_b128 v6, v[136:139] offset:272
	ds_write_b128 v6, v[140:143] offset:544
	ds_write_b128 v6, v[144:147] offset:816
	ds_write_b128 v6, v[148:151] offset:1088
	ds_write_b128 v6, v[152:155] offset:1360
	ds_write_b128 v6, v[156:159] offset:1632
	ds_write_b128 v6, v[160:163] offset:1904
.Luin_qskip:
	s_lshr_b32 s16, s12, 2
	s_lshl_b32 s16, s16, 8
	s_lshl_b32 s17, s14, 16
	s_add_u32 s16, s16, s17
	s_add_u32 s24, s6, s16
	s_addc_u32 s25, s7, 0
	s_waitcnt lgkmcnt(0)
	s_barrier
	v_and_b32_e32 v126, 15, v0
	v_lshrrev_b32_e32 v126, 2, v126
	v_cmp_eq_u32_e32 vcc, s30, v126
	s_and_saveexec_b64 s[22:23], vcc
	ds_read_b128 v[172:175], v7
	s_waitcnt lgkmcnt(0)
	global_store_dwordx4 v164, v[172:175], s[24:25]
	s_nop 1
	s_add_u32 s24, s24, 0x200000
	s_addc_u32 s25, s25, 0
	ds_read_b128 v[172:175], v7 offset:8704
	s_waitcnt lgkmcnt(0)
	global_store_dwordx4 v164, v[172:175], s[24:25]
	s_nop 1
	s_add_u32 s24, s24, 0x200000
	s_addc_u32 s25, s25, 0
	ds_read_b128 v[172:175], v7 offset:17408
	s_waitcnt lgkmcnt(0)
	global_store_dwordx4 v164, v[172:175], s[24:25]
	s_nop 1
	s_add_u32 s24, s24, 0x200000
	s_addc_u32 s25, s25, 0
	ds_read_b128 v[172:175], v7 offset:26112
	s_waitcnt lgkmcnt(0)
	global_store_dwordx4 v164, v[172:175], s[24:25]
	s_nop 1
	s_add_u32 s24, s24, 0x200000
	s_addc_u32 s25, s25, 0
	ds_read_b128 v[172:175], v7 offset:34816
	s_waitcnt lgkmcnt(0)
	global_store_dwordx4 v164, v[172:175], s[24:25]
	s_nop 1
	s_add_u32 s24, s24, 0x200000
	s_addc_u32 s25, s25, 0
	ds_read_b128 v[172:175], v7 offset:43520
	s_waitcnt lgkmcnt(0)
	global_store_dwordx4 v164, v[172:175], s[24:25]
	s_nop 1
	s_add_u32 s24, s24, 0x200000
	s_addc_u32 s25, s25, 0
	ds_read_b128 v[172:175], v7 offset:52224
	s_waitcnt lgkmcnt(0)
	global_store_dwordx4 v164, v[172:175], s[24:25]
	s_nop 1
	s_add_u32 s24, s24, 0x200000
	s_addc_u32 s25, s25, 0
	ds_read_b128 v[172:175], v7 offset:60928
	s_waitcnt lgkmcnt(0)
	global_store_dwordx4 v164, v[172:175], s[24:25]
	s_nop 1
	s_mov_b64 exec, s[22:23]
	s_barrier
	s_branch .LBB0_506
